# rebalanced split: 256 more conversion items go to the queue beside P1/P2 (2560 of 3072), P6 keeps two or three per light workgroup and none on workgroups with an extra GEMM unit
# baseline (speedup 1.0000x reference)
.LBB0_184:
	s_or_b64 exec, exec, s[0:1]
	s_add_u32 s2, s90, 0x2a800000
	s_addc_u32 s3, s91, 0
	s_add_u32 s16, s90, 0x4a800000
	v_readlane_b32 s6, v255, 25
	s_addc_u32 s17, s91, 0
	s_lshr_b32 s18, s6, 8
	v_readlane_b32 s0, v255, 4
	s_lshl_b32 s7, s18, 3
	s_waitcnt lgkmcnt(0)
	s_barrier
	s_mov_b32 s27, 0
	s_mov_b32 s32, s74
	s_mov_b32 s33, s75
	s_mov_b32 s34, s78
	s_mov_b32 s35, s79
	s_mov_b32 s36, s82
	s_mov_b32 s37, s83
	s_mov_b32 s42, s90
	s_mov_b32 s43, s91
	s_mov_b32 s95, 0xa00

.LBB0_266:
	s_and_b64 vcc, exec, s[0:1]
	s_mov_b64 s[0:1], -1
	s_cbranch_vccnz .LBB0_276
	s_mov_b32 s27, 1
	s_mov_b32 s32, s74
	s_mov_b32 s33, s75
	s_mov_b32 s34, s78
	s_mov_b32 s35, s79
	s_mov_b32 s36, s82
	s_mov_b32 s37, s83
	s_mov_b32 s42, s90
	s_mov_b32 s43, s91
	s_mov_b32 s95, 0xa00
	s_branch .Lcva_entry

.LBB0_562:
	v_writelane_b32 v255, s72, 31
	s_cmp_gt_i32 s14, 5
	s_cselect_b64 s[0:1], -1, 0
	v_writelane_b32 v255, s73, 32
	v_writelane_b32 v255, s74, 33
	v_writelane_b32 v255, s75, 34
	v_writelane_b32 v255, s76, 35
	v_writelane_b32 v255, s77, 36
	v_writelane_b32 v255, s78, 37
	v_writelane_b32 v255, s79, 38
	v_writelane_b32 v255, s80, 39
	v_writelane_b32 v255, s81, 40
	v_writelane_b32 v255, s82, 41
	v_writelane_b32 v255, s83, 42
	s_cmp_lt_i32 s15, 6
	v_writelane_b32 v255, s84, 43
	s_cselect_b64 s[2:3], -1, 0
	v_writelane_b32 v255, s85, 44
	s_or_b64 s[0:1], s[0:1], s[2:3]
	v_writelane_b32 v255, s86, 45
	s_and_b64 vcc, exec, s[0:1]
	v_writelane_b32 v255, s87, 46
	s_cbranch_vccnz .LBB0_654
	s_waitcnt vmcnt(11)
	v_mbcnt_lo_u32_b32 v0, -1, 0
	v_mbcnt_hi_u32_b32 v0, -1, v0
	v_readlane_b32 s0, v255, 4
	v_mov_b32_e32 v56, 1
	s_nop 0
	v_add_u32_e32 v0, s0, v0
	s_nop 0
	v_cmp_eq_u32_e32 vcc, 0, v0
	s_and_saveexec_b64 s[0:1], vcc
	s_cbranch_execz .LBB0_565
	v_mov_b32_e32 v0, 0
	global_load_dword v0, v0, s[90:91] offset:1024 sc1
	s_movk_i32 s2, 0xa00
	s_waitcnt vmcnt(0)
	v_cmp_gt_u32_e32 vcc, s2, v0
	s_nop 1
	v_cndmask_b32_e64 v56, 0, 1, vcc

.LBB0_598:
	s_or_b64 exec, exec, s[6:7]
	s_waitcnt lgkmcnt(0)
	s_barrier
	v_mov_b32_e32 v0, s17
	ds_read_b32 v0, v0
	s_waitcnt lgkmcnt(0)
	s_barrier
	s_mov_b64 s[6:7], -1
	s_waitcnt lgkmcnt(0)
	v_readfirstlane_b32 s12, v0
	s_cmpk_gt_u32 s12, 0x9ff
	s_cbranch_scc1 .LBB0_593
	s_lshr_b32 s10, s12, 10
	s_bfe_u32 s13, s12, 0x50005
	s_cmp_eq_u32 s10, 1
	s_cselect_b32 s6, s78, s82
	s_cselect_b32 s7, s79, s83
	s_cmpk_lt_u32 s12, 0x400
	s_cselect_b32 s7, s75, s7
	s_cselect_b32 s6, s74, s6
	s_lshl_b32 s66, s13, 22
	s_lshl_b32 s8, s13, 24
	s_add_u32 s67, s6, s8
	s_addc_u32 s68, s7, 0
	s_lshl_b32 s6, s12, 6
	s_and_b32 s11, s6, 0x780
	s_and_b32 s6, s12, 30
	s_add_i32 s6, s6, s16
	s_lshl_b32 s8, s6, 6
	s_lshl_b64 s[6:7], s[8:9], 13
	s_add_u32 s6, s67, s6
	s_addc_u32 s7, s68, s7
	s_lshl_b32 s8, s12, 10
	s_and_b32 s8, s8, 0x400
	s_lshl_b32 s12, s8, 2
	s_add_u32 s6, s6, s12
	s_addc_u32 s7, s7, 0
	s_add_u32 s6, s6, s18
	s_addc_u32 s7, s7, 0
	v_lshl_add_u64 v[100:101], s[6:7], 0, v[96:97]
	s_movk_i32 s12, 0x2000
	v_add_co_u32_e32 v0, vcc, s12, v100
	s_movk_i32 s12, 0x4000
	s_nop 0
	v_addc_co_u32_e32 v1, vcc, 0, v101, vcc
	v_add_co_u32_e32 v2, vcc, s12, v100
	s_movk_i32 s12, 0x6000
	s_nop 0
	v_addc_co_u32_e32 v3, vcc, 0, v101, vcc
	global_load_dwordx4 v[16:19], v[0:1], off nt
	global_load_dwordx4 v[24:27], v[2:3], off nt
	v_add_co_u32_e32 v0, vcc, s12, v100
	s_mov_b32 s12, 0x8000
	s_nop 0
	v_addc_co_u32_e32 v1, vcc, 0, v101, vcc
	v_add_co_u32_e32 v2, vcc, s12, v100
	s_mov_b32 s12, 0xa000
	s_nop 0
	v_addc_co_u32_e32 v3, vcc, 0, v101, vcc
	global_load_dwordx4 v[52:55], v[0:1], off nt
	global_load_dwordx4 v[44:47], v[2:3], off nt
	v_add_co_u32_e32 v0, vcc, s12, v100
	s_mov_b32 s12, 0xc000
	s_nop 0
	v_addc_co_u32_e32 v1, vcc, 0, v101, vcc
	v_add_co_u32_e32 v2, vcc, s12, v100
	s_mov_b32 s12, 0xe000
	s_nop 0
	v_addc_co_u32_e32 v3, vcc, 0, v101, vcc
	global_load_dwordx4 v[64:67], v[0:1], off nt
	global_load_dwordx4 v[72:75], v[2:3], off nt
	v_add_co_u32_e32 v0, vcc, s12, v100
	s_mov_b32 s12, 0x10000
	s_nop 0
	v_addc_co_u32_e32 v1, vcc, 0, v101, vcc
	v_add_co_u32_e32 v2, vcc, s12, v100
	s_mov_b32 s12, 0x12000
	s_nop 0
	v_addc_co_u32_e32 v3, vcc, 0, v101, vcc
	global_load_dwordx4 v[80:83], v[0:1], off nt
	global_load_dwordx4 v[20:23], v[2:3], off nt
	v_add_co_u32_e32 v0, vcc, s12, v100
	s_mov_b32 s12, 0x14000
	s_nop 0
	v_addc_co_u32_e32 v1, vcc, 0, v101, vcc
	v_add_co_u32_e32 v2, vcc, s12, v100
	s_mov_b32 s12, 0x16000
	s_nop 0
	v_addc_co_u32_e32 v3, vcc, 0, v101, vcc
	global_load_dwordx4 v[28:31], v[0:1], off nt
	global_load_dwordx4 v[48:51], v[2:3], off nt
	v_add_co_u32_e32 v0, vcc, s12, v100
	s_mov_b32 s12, 0x18000
	s_nop 0
	v_addc_co_u32_e32 v1, vcc, 0, v101, vcc
	v_add_co_u32_e32 v2, vcc, s12, v100
	s_mov_b32 s12, 0x1a000
	s_nop 0
	v_addc_co_u32_e32 v3, vcc, 0, v101, vcc
	global_load_dwordx4 v[68:71], v[0:1], off nt
	global_load_dwordx4 v[56:59], v[2:3], off nt
	v_add_co_u32_e32 v0, vcc, s12, v100
	s_mov_b32 s12, 0x1c000
	s_nop 0
	v_addc_co_u32_e32 v1, vcc, 0, v101, vcc
	v_add_co_u32_e32 v2, vcc, s12, v100
	s_mov_b32 s12, 0x1e000
	s_nop 0
	v_addc_co_u32_e32 v3, vcc, 0, v101, vcc
	global_load_dwordx4 v[76:79], v[0:1], off nt
	global_load_dwordx4 v[84:87], v[2:3], off nt
	v_add_co_u32_e32 v0, vcc, s12, v100
	s_mov_b32 s12, 0x20000
	s_nop 0
	v_addc_co_u32_e32 v1, vcc, 0, v101, vcc
	v_add_co_u32_e32 v2, vcc, s12, v100
	s_mov_b32 s12, 0x22000
	s_nop 0
	v_addc_co_u32_e32 v3, vcc, 0, v101, vcc
	v_add_co_u32_e32 v4, vcc, s12, v100
	global_load_dwordx4 v[92:95], v[0:1], off nt
	s_nop 0
	global_load_dwordx4 v[0:3], v[2:3], off nt
	v_addc_co_u32_e32 v5, vcc, 0, v101, vcc
	v_add_co_u32_e32 v8, vcc, s19, v100
	s_nop 1
	v_addc_co_u32_e32 v9, vcc, 0, v101, vcc
	v_add_co_u32_e32 v12, vcc, s20, v100
	global_load_dwordx4 v[4:7], v[4:5], off nt
	s_nop 0
	global_load_dwordx4 v[8:11], v[8:9], off nt
	v_addc_co_u32_e32 v13, vcc, 0, v101, vcc
	v_add_co_u32_e32 v14, vcc, s21, v100
	s_nop 1
	v_addc_co_u32_e32 v15, vcc, 0, v101, vcc
	v_add_co_u32_e32 v36, vcc, s22, v100
	global_load_dwordx4 v[32:35], v[12:13], off nt
	s_nop 0
	global_load_dwordx4 v[12:15], v[14:15], off nt
	v_addc_co_u32_e32 v37, vcc, 0, v101, vcc
	v_add_co_u32_e32 v40, vcc, s23, v100
	s_nop 1
	v_addc_co_u32_e32 v41, vcc, 0, v101, vcc
	v_add_co_u32_e32 v60, vcc, s24, v100
	global_load_dwordx4 v[36:39], v[36:37], off nt
	s_nop 0
	global_load_dwordx4 v[40:43], v[40:41], off nt
	v_addc_co_u32_e32 v61, vcc, 0, v101, vcc
	global_load_dwordx4 v[88:91], v96, s[6:7] nt
	s_nop 0
	global_load_dwordx4 v[60:63], v[60:61], off nt
	s_lshl_b32 s6, s13, 23
	s_add_u32 s13, s2, s6
	s_addc_u32 s12, s3, 0
	s_add_u32 s66, s14, s66
	s_addc_u32 s67, s15, 0
	s_cmp_eq_u32 s10, 2
	s_cselect_b64 vcc, -1, 0
	s_and_b64 s[6:7], vcc, exec
	s_cselect_b32 s12, s67, s12
	s_cselect_b32 s13, s66, s13
	s_waitcnt vmcnt(1)
	v_mul_f32_e32 v88, 0x42800000, v88
	v_mul_f32_e32 v16, 0x42800000, v16
	v_mov_b32_e32 v158, v97
	v_cvt_pk_fp8_f32 v158, v88, v16
	v_mul_f32_e32 v24, 0x42800000, v24
	v_mul_f32_e32 v52, 0x42800000, v52
	v_mul_f32_e32 v16, 0x42800000, v44
	v_cvt_pk_fp8_f32 v158, v24, v52 op_sel:[0,0,1]
	v_mul_f32_e32 v24, 0x42800000, v64
	v_mov_b32_e32 v159, v97
	v_cvt_pk_fp8_f32 v159, v16, v24
	v_mul_f32_e32 v24, 0x42800000, v89
	v_mul_f32_e32 v17, 0x42800000, v17
	v_mov_b32_e32 v16, v97
	v_cvt_pk_fp8_f32 v16, v24, v17
	v_mul_f32_e32 v44, 0x42800000, v72
	v_mul_f32_e32 v52, 0x42800000, v80
	v_cvt_pk_fp8_f32 v159, v44, v52 op_sel:[0,0,1]
	v_mul_f32_e32 v25, 0x42800000, v25
	v_mul_f32_e32 v44, 0x42800000, v53
	v_cvt_pk_fp8_f32 v16, v25, v44 op_sel:[0,0,1]
	v_mul_f32_e32 v24, 0x42800000, v45
	v_mul_f32_e32 v25, 0x42800000, v65
	v_mov_b32_e32 v17, v97
	v_cvt_pk_fp8_f32 v17, v24, v25
	v_mul_f32_e32 v44, 0x42800000, v73
	v_mul_f32_e32 v45, 0x42800000, v81
	v_mul_f32_e32 v18, 0x42800000, v18
	v_cvt_pk_fp8_f32 v17, v44, v45 op_sel:[0,0,1]
	v_mul_f32_e32 v24, 0x42800000, v26
	v_mul_f32_e32 v25, 0x42800000, v54
	v_mul_f32_e32 v19, 0x42800000, v19
	ds_write2_b64 v134, v[158:159], v[16:17] offset1:16
	v_mul_f32_e32 v17, 0x42800000, v90
	v_mov_b32_e32 v16, v97
	v_cvt_pk_fp8_f32 v16, v17, v18
	v_mul_f32_e32 v18, 0x42800000, v46
	v_mov_b32_e32 v17, v97
	v_mul_f32_e32 v26, 0x42800000, v82
	v_cvt_pk_fp8_f32 v16, v24, v25 op_sel:[0,0,1]
	v_mul_f32_e32 v24, 0x42800000, v66
	v_cvt_pk_fp8_f32 v17, v18, v24
	v_mul_f32_e32 v24, 0x42800000, v91
	v_mov_b32_e32 v18, v97
	v_cvt_pk_fp8_f32 v18, v24, v19
	v_mul_f32_e32 v25, 0x42800000, v74
	v_cvt_pk_fp8_f32 v17, v25, v26 op_sel:[0,0,1]
	v_mul_f32_e32 v25, 0x42800000, v27
	v_mul_f32_e32 v26, 0x42800000, v55
	v_cvt_pk_fp8_f32 v18, v25, v26 op_sel:[0,0,1]
	v_mul_f32_e32 v24, 0x42800000, v47
	v_mul_f32_e32 v25, 0x42800000, v67
	v_mov_b32_e32 v19, v97
	v_cvt_pk_fp8_f32 v19, v24, v25
	v_mul_f32_e32 v26, 0x42800000, v75
	v_mul_f32_e32 v27, 0x42800000, v83
	v_cvt_pk_fp8_f32 v19, v26, v27 op_sel:[0,0,1]
	ds_write2_b64 v134, v[16:17], v[18:19] offset0:32 offset1:48
	v_add_co_u32_e64 v16, s[6:7], s25, v100
	s_nop 1
	v_addc_co_u32_e64 v17, s[6:7], 0, v101, s[6:7]
	v_add_co_u32_e64 v24, s[6:7], s26, v100
	s_nop 1
	v_addc_co_u32_e64 v25, s[6:7], 0, v101, s[6:7]
	v_add_co_u32_e64 v44, s[6:7], s27, v100
	global_load_dwordx4 v[16:19], v[16:17], off nt
	s_nop 0
	global_load_dwordx4 v[24:27], v[24:25], off nt
	v_addc_co_u32_e64 v45, s[6:7], 0, v101, s[6:7]
	v_add_co_u32_e64 v52, s[6:7], s28, v100
	s_nop 1
	v_addc_co_u32_e64 v53, s[6:7], 0, v101, s[6:7]
	global_load_dwordx4 v[44:47], v[44:45], off nt
	s_nop 0
	global_load_dwordx4 v[64:67], v[52:53], off nt
	v_add_co_u32_e64 v52, s[6:7], s29, v100
	s_nop 1
	v_addc_co_u32_e64 v53, s[6:7], 0, v101, s[6:7]
	v_add_co_u32_e64 v72, s[6:7], s30, v100
	s_nop 1
	v_addc_co_u32_e64 v73, s[6:7], 0, v101, s[6:7]
	v_add_co_u32_e64 v80, s[6:7], s31, v100
	global_load_dwordx4 v[52:55], v[52:53], off nt
	s_nop 0
	global_load_dwordx4 v[72:75], v[72:73], off nt
	v_addc_co_u32_e64 v81, s[6:7], 0, v101, s[6:7]
	v_add_co_u32_e64 v88, s[6:7], s33, v100
	s_nop 1
	v_addc_co_u32_e64 v89, s[6:7], 0, v101, s[6:7]
	global_load_dwordx4 v[80:83], v[80:81], off nt
	s_nop 0
	global_load_dwordx4 v[88:91], v[88:89], off nt
	v_mul_f32_e32 v20, 0x42800000, v20
	v_mul_f32_e32 v28, 0x42800000, v28
	v_mov_b32_e32 v158, v97
	v_cvt_pk_fp8_f32 v158, v20, v28
	v_mul_f32_e32 v20, 0x42800000, v56
	v_mul_f32_e32 v28, 0x42800000, v76
	v_mov_b32_e32 v159, v97
	v_cvt_pk_fp8_f32 v159, v20, v28
	v_mul_f32_e32 v21, 0x42800000, v21
	v_mul_f32_e32 v28, 0x42800000, v29
	v_mov_b32_e32 v20, v97
	v_cvt_pk_fp8_f32 v20, v21, v28
	v_mul_f32_e32 v48, 0x42800000, v48
	v_mul_f32_e32 v68, 0x42800000, v68
	v_cvt_pk_fp8_f32 v158, v48, v68 op_sel:[0,0,1]
	v_mul_f32_e32 v48, 0x42800000, v84
	v_mul_f32_e32 v56, 0x42800000, v92
	v_cvt_pk_fp8_f32 v159, v48, v56 op_sel:[0,0,1]
	v_mul_f32_e32 v29, 0x42800000, v49
	v_mul_f32_e32 v48, 0x42800000, v69
	v_cvt_pk_fp8_f32 v20, v29, v48 op_sel:[0,0,1]
	v_mul_f32_e32 v28, 0x42800000, v57
	v_mul_f32_e32 v29, 0x42800000, v77
	v_mov_b32_e32 v21, v97
	v_cvt_pk_fp8_f32 v21, v28, v29
	v_mul_f32_e32 v48, 0x42800000, v85
	v_mul_f32_e32 v49, 0x42800000, v93
	v_mul_f32_e32 v28, 0x42800000, v50
	v_cvt_pk_fp8_f32 v21, v48, v49 op_sel:[0,0,1]
	v_mul_f32_e32 v29, 0x42800000, v70
	v_mul_f32_e32 v23, 0x42800000, v23
	ds_write2_b64 v135, v[158:159], v[20:21] offset1:16
	v_mul_f32_e32 v21, 0x42800000, v22
	v_mul_f32_e32 v22, 0x42800000, v30
	v_mov_b32_e32 v20, v97
	v_cvt_pk_fp8_f32 v20, v21, v22
	v_mul_f32_e32 v22, 0x42800000, v58
	v_mov_b32_e32 v21, v97
	v_mul_f32_e32 v30, 0x42800000, v94
	v_cvt_pk_fp8_f32 v20, v28, v29 op_sel:[0,0,1]
	v_mul_f32_e32 v28, 0x42800000, v78
	v_cvt_pk_fp8_f32 v21, v22, v28
	v_mul_f32_e32 v28, 0x42800000, v31
	v_mov_b32_e32 v22, v97
	v_cvt_pk_fp8_f32 v22, v23, v28
	v_mul_f32_e32 v29, 0x42800000, v86
	v_cvt_pk_fp8_f32 v21, v29, v30 op_sel:[0,0,1]
	v_mul_f32_e32 v29, 0x42800000, v51
	v_mul_f32_e32 v30, 0x42800000, v71
	v_cvt_pk_fp8_f32 v22, v29, v30 op_sel:[0,0,1]
	v_mul_f32_e32 v28, 0x42800000, v59
	v_mul_f32_e32 v29, 0x42800000, v79
	v_mov_b32_e32 v23, v97
	v_cvt_pk_fp8_f32 v23, v28, v29
	v_mul_f32_e32 v30, 0x42800000, v87
	v_mul_f32_e32 v31, 0x42800000, v95
	v_cvt_pk_fp8_f32 v23, v30, v31 op_sel:[0,0,1]
	ds_write2_b64 v135, v[20:21], v[22:23] offset0:32 offset1:48
	v_add_co_u32_e64 v20, s[6:7], s34, v100
	s_nop 1
	v_addc_co_u32_e64 v21, s[6:7], 0, v101, s[6:7]
	v_add_co_u32_e64 v28, s[6:7], s35, v100
	s_nop 1
	v_addc_co_u32_e64 v29, s[6:7], 0, v101, s[6:7]
	v_add_co_u32_e64 v48, s[6:7], s36, v100
	global_load_dwordx4 v[20:23], v[20:21], off nt
	s_nop 0
	global_load_dwordx4 v[28:31], v[28:29], off nt
	v_addc_co_u32_e64 v49, s[6:7], 0, v101, s[6:7]
	v_add_co_u32_e64 v56, s[6:7], s37, v100
	s_nop 1
	v_addc_co_u32_e64 v57, s[6:7], 0, v101, s[6:7]
	global_load_dwordx4 v[48:51], v[48:49], off nt
	s_nop 0
	global_load_dwordx4 v[68:71], v[56:57], off nt
	v_add_co_u32_e64 v56, s[6:7], s38, v100
	s_nop 1
	v_addc_co_u32_e64 v57, s[6:7], 0, v101, s[6:7]
	v_add_co_u32_e64 v76, s[6:7], s39, v100
	s_nop 1
	v_addc_co_u32_e64 v77, s[6:7], 0, v101, s[6:7]
	v_add_co_u32_e64 v84, s[6:7], s40, v100
	global_load_dwordx4 v[56:59], v[56:57], off nt
	s_nop 0
	global_load_dwordx4 v[76:79], v[76:77], off nt
	v_addc_co_u32_e64 v85, s[6:7], 0, v101, s[6:7]
	v_add_co_u32_e64 v92, s[6:7], s41, v100
	s_nop 1
	v_addc_co_u32_e64 v93, s[6:7], 0, v101, s[6:7]
	global_load_dwordx4 v[84:87], v[84:85], off nt
	s_nop 0
	global_load_dwordx4 v[92:95], v[92:93], off nt
	v_mul_f32_e32 v0, 0x42800000, v0
	v_mul_f32_e32 v4, 0x42800000, v4
	v_mov_b32_e32 v158, v97
	v_cvt_pk_fp8_f32 v158, v0, v4
	v_mul_f32_e32 v0, 0x42800000, v12
	v_mul_f32_e32 v4, 0x42800000, v36
	v_mov_b32_e32 v159, v97
	v_cvt_pk_fp8_f32 v159, v0, v4
	v_mul_f32_e32 v1, 0x42800000, v1
	v_mul_f32_e32 v4, 0x42800000, v5
	v_mov_b32_e32 v0, v97
	v_cvt_pk_fp8_f32 v0, v1, v4
	v_mul_f32_e32 v8, 0x42800000, v8
	v_mul_f32_e32 v32, 0x42800000, v32
	v_cvt_pk_fp8_f32 v158, v8, v32 op_sel:[0,0,1]
	v_mul_f32_e32 v8, 0x42800000, v40
	s_waitcnt vmcnt(16)
	v_mul_f32_e32 v12, 0x42800000, v60
	v_cvt_pk_fp8_f32 v159, v8, v12 op_sel:[0,0,1]
	v_mul_f32_e32 v5, 0x42800000, v9
	v_mul_f32_e32 v8, 0x42800000, v33
	v_cvt_pk_fp8_f32 v0, v5, v8 op_sel:[0,0,1]
	v_mul_f32_e32 v4, 0x42800000, v13
	v_mul_f32_e32 v5, 0x42800000, v37
	v_mov_b32_e32 v1, v97
	v_cvt_pk_fp8_f32 v1, v4, v5
	v_mul_f32_e32 v8, 0x42800000, v41
	v_mul_f32_e32 v9, 0x42800000, v61
	v_mul_f32_e32 v4, 0x42800000, v10
	v_cvt_pk_fp8_f32 v1, v8, v9 op_sel:[0,0,1]
	v_mul_f32_e32 v5, 0x42800000, v34
	v_mul_f32_e32 v3, 0x42800000, v3
	ds_write2_b64 v136, v[158:159], v[0:1] offset1:16
	v_mul_f32_e32 v1, 0x42800000, v2
	v_mul_f32_e32 v2, 0x42800000, v6
	v_mov_b32_e32 v0, v97
	v_cvt_pk_fp8_f32 v0, v1, v2
	v_mul_f32_e32 v2, 0x42800000, v14
	v_mov_b32_e32 v1, v97
	v_mul_f32_e32 v6, 0x42800000, v62
	v_cvt_pk_fp8_f32 v0, v4, v5 op_sel:[0,0,1]
	v_mul_f32_e32 v4, 0x42800000, v38
	v_cvt_pk_fp8_f32 v1, v2, v4
	v_mul_f32_e32 v4, 0x42800000, v7
	v_mov_b32_e32 v2, v97
	v_cvt_pk_fp8_f32 v2, v3, v4
	v_mul_f32_e32 v5, 0x42800000, v42
	v_cvt_pk_fp8_f32 v1, v5, v6 op_sel:[0,0,1]
	v_mul_f32_e32 v5, 0x42800000, v11
	v_mul_f32_e32 v6, 0x42800000, v35
	v_cvt_pk_fp8_f32 v2, v5, v6 op_sel:[0,0,1]
	v_mul_f32_e32 v4, 0x42800000, v15
	v_mul_f32_e32 v5, 0x42800000, v39
	v_mov_b32_e32 v3, v97
	v_cvt_pk_fp8_f32 v3, v4, v5
	v_mul_f32_e32 v6, 0x42800000, v43
	v_mul_f32_e32 v7, 0x42800000, v63
	v_cvt_pk_fp8_f32 v3, v6, v7 op_sel:[0,0,1]
	ds_write2_b64 v136, v[0:1], v[2:3] offset0:32 offset1:48
	v_add_co_u32_e64 v0, s[6:7], s42, v100
	s_nop 1
	v_addc_co_u32_e64 v1, s[6:7], 0, v101, s[6:7]
	v_add_co_u32_e64 v4, s[6:7], s43, v100
	s_nop 1
	v_addc_co_u32_e64 v5, s[6:7], 0, v101, s[6:7]
	v_add_co_u32_e64 v8, s[6:7], s44, v100
	global_load_dwordx4 v[0:3], v[0:1], off nt
	s_nop 0
	global_load_dwordx4 v[4:7], v[4:5], off nt
	v_addc_co_u32_e64 v9, s[6:7], 0, v101, s[6:7]
	v_add_co_u32_e64 v12, s[6:7], s45, v100
	s_nop 1
	v_addc_co_u32_e64 v13, s[6:7], 0, v101, s[6:7]
	global_load_dwordx4 v[8:11], v[8:9], off nt
	s_nop 0
	global_load_dwordx4 v[32:35], v[12:13], off nt
	v_add_co_u32_e64 v12, s[6:7], s46, v100
	s_nop 1
	v_addc_co_u32_e64 v13, s[6:7], 0, v101, s[6:7]
	v_add_co_u32_e64 v36, s[6:7], s47, v100
	s_nop 1
	v_addc_co_u32_e64 v37, s[6:7], 0, v101, s[6:7]
	v_add_co_u32_e64 v40, s[6:7], s48, v100
	global_load_dwordx4 v[12:15], v[12:13], off nt
	s_nop 0
	global_load_dwordx4 v[36:39], v[36:37], off nt
	v_addc_co_u32_e64 v41, s[6:7], 0, v101, s[6:7]
	v_add_co_u32_e64 v60, s[6:7], s49, v100
	s_nop 1
	v_addc_co_u32_e64 v61, s[6:7], 0, v101, s[6:7]
	global_load_dwordx4 v[40:43], v[40:41], off nt
	s_nop 0
	global_load_dwordx4 v[60:63], v[60:61], off nt
	s_waitcnt vmcnt(23)
	v_mul_f32_e32 v16, 0x42800000, v16
	s_waitcnt vmcnt(22)
	v_mul_f32_e32 v24, 0x42800000, v24
	v_mov_b32_e32 v158, v97
	v_cvt_pk_fp8_f32 v158, v16, v24
	s_waitcnt vmcnt(19)
	v_mul_f32_e32 v16, 0x42800000, v52
	s_waitcnt vmcnt(18)
	v_mul_f32_e32 v24, 0x42800000, v72
	v_mov_b32_e32 v159, v97
	v_cvt_pk_fp8_f32 v159, v16, v24
	v_mul_f32_e32 v17, 0x42800000, v17
	v_mul_f32_e32 v24, 0x42800000, v25
	v_mov_b32_e32 v16, v97
	v_cvt_pk_fp8_f32 v16, v17, v24
	v_mul_f32_e32 v44, 0x42800000, v44
	v_mul_f32_e32 v64, 0x42800000, v64
	v_cvt_pk_fp8_f32 v158, v44, v64 op_sel:[0,0,1]
	s_waitcnt vmcnt(17)
	v_mul_f32_e32 v44, 0x42800000, v80
	s_waitcnt vmcnt(16)
	v_mul_f32_e32 v52, 0x42800000, v88
	v_cvt_pk_fp8_f32 v159, v44, v52 op_sel:[0,0,1]
	v_mul_f32_e32 v25, 0x42800000, v45
	v_mul_f32_e32 v44, 0x42800000, v65
	v_cvt_pk_fp8_f32 v16, v25, v44 op_sel:[0,0,1]
	v_mul_f32_e32 v24, 0x42800000, v53
	v_mul_f32_e32 v25, 0x42800000, v73
	v_mov_b32_e32 v17, v97
	v_cvt_pk_fp8_f32 v17, v24, v25
	v_mul_f32_e32 v44, 0x42800000, v81
	v_mul_f32_e32 v45, 0x42800000, v89
	v_mul_f32_e32 v24, 0x42800000, v46
	v_cvt_pk_fp8_f32 v17, v44, v45 op_sel:[0,0,1]
	v_mul_f32_e32 v25, 0x42800000, v66
	v_mul_f32_e32 v19, 0x42800000, v19
	ds_write2_b64 v137, v[158:159], v[16:17] offset1:16
	v_mul_f32_e32 v17, 0x42800000, v18
	v_mul_f32_e32 v18, 0x42800000, v26
	v_mov_b32_e32 v16, v97
	v_cvt_pk_fp8_f32 v16, v17, v18
	v_mul_f32_e32 v18, 0x42800000, v54
	v_mov_b32_e32 v17, v97
	v_mul_f32_e32 v26, 0x42800000, v90
	v_cvt_pk_fp8_f32 v16, v24, v25 op_sel:[0,0,1]
	v_mul_f32_e32 v24, 0x42800000, v74
	v_cvt_pk_fp8_f32 v17, v18, v24
	v_mul_f32_e32 v24, 0x42800000, v27
	v_mov_b32_e32 v18, v97
	v_cvt_pk_fp8_f32 v18, v19, v24
	v_mul_f32_e32 v25, 0x42800000, v82
	v_cvt_pk_fp8_f32 v17, v25, v26 op_sel:[0,0,1]
	v_mul_f32_e32 v25, 0x42800000, v47
	v_mul_f32_e32 v26, 0x42800000, v67
	v_cvt_pk_fp8_f32 v18, v25, v26 op_sel:[0,0,1]
	v_mul_f32_e32 v24, 0x42800000, v55
	v_mul_f32_e32 v25, 0x42800000, v75
	v_mov_b32_e32 v19, v97
	v_cvt_pk_fp8_f32 v19, v24, v25
	v_mul_f32_e32 v26, 0x42800000, v83
	v_mul_f32_e32 v27, 0x42800000, v91
	v_cvt_pk_fp8_f32 v19, v26, v27 op_sel:[0,0,1]
	ds_write2_b64 v137, v[16:17], v[18:19] offset0:32 offset1:48
	v_add_co_u32_e64 v16, s[6:7], s50, v100
	s_nop 1
	v_addc_co_u32_e64 v17, s[6:7], 0, v101, s[6:7]
	v_add_co_u32_e64 v24, s[6:7], s51, v100
	s_nop 1
	v_addc_co_u32_e64 v25, s[6:7], 0, v101, s[6:7]
	v_add_co_u32_e64 v44, s[6:7], s52, v100
	global_load_dwordx4 v[16:19], v[16:17], off nt
	s_nop 0
	global_load_dwordx4 v[24:27], v[24:25], off nt
	v_addc_co_u32_e64 v45, s[6:7], 0, v101, s[6:7]
	v_add_co_u32_e64 v52, s[6:7], s53, v100
	s_nop 1
	v_addc_co_u32_e64 v53, s[6:7], 0, v101, s[6:7]
	global_load_dwordx4 v[44:47], v[44:45], off nt
	s_nop 0
	global_load_dwordx4 v[64:67], v[52:53], off nt
	v_add_co_u32_e64 v52, s[6:7], s54, v100
	s_nop 1
	v_addc_co_u32_e64 v53, s[6:7], 0, v101, s[6:7]
	v_add_co_u32_e64 v72, s[6:7], s55, v100
	s_nop 1
	v_addc_co_u32_e64 v73, s[6:7], 0, v101, s[6:7]
	v_add_co_u32_e64 v80, s[6:7], s56, v100
	global_load_dwordx4 v[52:55], v[52:53], off nt
	s_nop 0
	global_load_dwordx4 v[72:75], v[72:73], off nt
	v_addc_co_u32_e64 v81, s[6:7], 0, v101, s[6:7]
	v_add_co_u32_e64 v88, s[6:7], s57, v100
	s_nop 1
	v_addc_co_u32_e64 v89, s[6:7], 0, v101, s[6:7]
	global_load_dwordx4 v[80:83], v[80:81], off nt
	s_nop 0
	global_load_dwordx4 v[88:91], v[88:89], off nt
	s_waitcnt vmcnt(23)
	v_mul_f32_e32 v20, 0x42800000, v20
	s_waitcnt vmcnt(22)
	v_mul_f32_e32 v28, 0x42800000, v28
	v_mov_b32_e32 v158, v97
	v_cvt_pk_fp8_f32 v158, v20, v28
	s_waitcnt vmcnt(19)
	v_mul_f32_e32 v20, 0x42800000, v56
	s_waitcnt vmcnt(18)
	v_mul_f32_e32 v28, 0x42800000, v76
	v_mov_b32_e32 v159, v97
	v_cvt_pk_fp8_f32 v159, v20, v28
	v_mul_f32_e32 v21, 0x42800000, v21
	v_mul_f32_e32 v28, 0x42800000, v29
	v_mov_b32_e32 v20, v97
	v_cvt_pk_fp8_f32 v20, v21, v28
	v_mul_f32_e32 v48, 0x42800000, v48
	v_mul_f32_e32 v68, 0x42800000, v68
	v_cvt_pk_fp8_f32 v158, v48, v68 op_sel:[0,0,1]
	s_waitcnt vmcnt(17)
	v_mul_f32_e32 v48, 0x42800000, v84
	s_waitcnt vmcnt(16)
	v_mul_f32_e32 v56, 0x42800000, v92
	v_cvt_pk_fp8_f32 v159, v48, v56 op_sel:[0,0,1]
	v_mul_f32_e32 v29, 0x42800000, v49
	v_mul_f32_e32 v48, 0x42800000, v69
	v_cvt_pk_fp8_f32 v20, v29, v48 op_sel:[0,0,1]
	v_mul_f32_e32 v28, 0x42800000, v57
	v_mul_f32_e32 v29, 0x42800000, v77
	v_mov_b32_e32 v21, v97
	v_cvt_pk_fp8_f32 v21, v28, v29
	v_mul_f32_e32 v48, 0x42800000, v85
	v_mul_f32_e32 v49, 0x42800000, v93
	v_mul_f32_e32 v28, 0x42800000, v50
	v_cvt_pk_fp8_f32 v21, v48, v49 op_sel:[0,0,1]
	v_mul_f32_e32 v29, 0x42800000, v70
	v_mul_f32_e32 v23, 0x42800000, v23
	ds_write2_b64 v138, v[158:159], v[20:21] offset1:16
	v_mul_f32_e32 v21, 0x42800000, v22
	v_mul_f32_e32 v22, 0x42800000, v30
	v_mov_b32_e32 v20, v97
	v_cvt_pk_fp8_f32 v20, v21, v22
	v_mul_f32_e32 v22, 0x42800000, v58
	v_mov_b32_e32 v21, v97
	v_mul_f32_e32 v30, 0x42800000, v94
	v_cvt_pk_fp8_f32 v20, v28, v29 op_sel:[0,0,1]
	v_mul_f32_e32 v28, 0x42800000, v78
	v_cvt_pk_fp8_f32 v21, v22, v28
	v_mul_f32_e32 v28, 0x42800000, v31
	v_mov_b32_e32 v22, v97
	v_cvt_pk_fp8_f32 v22, v23, v28
	v_mul_f32_e32 v29, 0x42800000, v86
	v_cvt_pk_fp8_f32 v21, v29, v30 op_sel:[0,0,1]
	v_mul_f32_e32 v29, 0x42800000, v51
	v_mul_f32_e32 v30, 0x42800000, v71
	v_cvt_pk_fp8_f32 v22, v29, v30 op_sel:[0,0,1]
	v_mul_f32_e32 v28, 0x42800000, v59
	v_mul_f32_e32 v29, 0x42800000, v79
	v_mov_b32_e32 v23, v97
	v_cvt_pk_fp8_f32 v23, v28, v29
	v_mul_f32_e32 v30, 0x42800000, v87
	v_mul_f32_e32 v31, 0x42800000, v95
	v_cvt_pk_fp8_f32 v23, v30, v31 op_sel:[0,0,1]
	ds_write2_b64 v138, v[20:21], v[22:23] offset0:32 offset1:48
	v_add_co_u32_e64 v20, s[6:7], s58, v100
	s_nop 1
	v_addc_co_u32_e64 v21, s[6:7], 0, v101, s[6:7]
	v_add_co_u32_e64 v28, s[6:7], s59, v100
	s_nop 1
	v_addc_co_u32_e64 v29, s[6:7], 0, v101, s[6:7]
	v_add_co_u32_e64 v48, s[6:7], s60, v100
	global_load_dwordx4 v[20:23], v[20:21], off nt
	s_nop 0
	global_load_dwordx4 v[28:31], v[28:29], off nt
	v_addc_co_u32_e64 v49, s[6:7], 0, v101, s[6:7]
	v_add_co_u32_e64 v56, s[6:7], s61, v100
	s_nop 1
	v_addc_co_u32_e64 v57, s[6:7], 0, v101, s[6:7]
	global_load_dwordx4 v[48:51], v[48:49], off nt
	s_nop 0
	global_load_dwordx4 v[68:71], v[56:57], off nt
	v_add_co_u32_e64 v56, s[6:7], s62, v100
	s_nop 1
	v_addc_co_u32_e64 v57, s[6:7], 0, v101, s[6:7]
	v_add_co_u32_e64 v76, s[6:7], s63, v100
	s_nop 1
	v_addc_co_u32_e64 v77, s[6:7], 0, v101, s[6:7]
	v_add_co_u32_e64 v84, s[6:7], s64, v100
	global_load_dwordx4 v[56:59], v[56:57], off nt
	s_nop 0
	global_load_dwordx4 v[76:79], v[76:77], off nt
	v_addc_co_u32_e64 v85, s[6:7], 0, v101, s[6:7]
	v_add_co_u32_e64 v92, s[6:7], s65, v100
	s_nop 1
	v_addc_co_u32_e64 v93, s[6:7], 0, v101, s[6:7]
	global_load_dwordx4 v[84:87], v[84:85], off nt
	s_nop 0
	global_load_dwordx4 v[92:95], v[92:93], off nt
	s_waitcnt vmcnt(23)
	v_mul_f32_e32 v0, 0x42800000, v0
	s_waitcnt vmcnt(22)
	v_mul_f32_e32 v4, 0x42800000, v4
	v_mov_b32_e32 v100, v97
	v_cvt_pk_fp8_f32 v100, v0, v4
	s_waitcnt vmcnt(19)
	v_mul_f32_e32 v0, 0x42800000, v12
	s_waitcnt vmcnt(18)
	v_mul_f32_e32 v4, 0x42800000, v36
	v_mov_b32_e32 v101, v97
	v_cvt_pk_fp8_f32 v101, v0, v4
	v_mul_f32_e32 v1, 0x42800000, v1
	v_mul_f32_e32 v4, 0x42800000, v5
	v_mov_b32_e32 v0, v97
	v_cvt_pk_fp8_f32 v0, v1, v4
	v_mul_f32_e32 v8, 0x42800000, v8
	v_mul_f32_e32 v32, 0x42800000, v32
	v_cvt_pk_fp8_f32 v100, v8, v32 op_sel:[0,0,1]
	s_waitcnt vmcnt(17)
	v_mul_f32_e32 v8, 0x42800000, v40
	s_waitcnt vmcnt(16)
	v_mul_f32_e32 v12, 0x42800000, v60
	v_cvt_pk_fp8_f32 v101, v8, v12 op_sel:[0,0,1]
	v_mul_f32_e32 v5, 0x42800000, v9
	v_mul_f32_e32 v8, 0x42800000, v33
	v_cvt_pk_fp8_f32 v0, v5, v8 op_sel:[0,0,1]
	v_mul_f32_e32 v4, 0x42800000, v13
	v_mul_f32_e32 v5, 0x42800000, v37
	v_mov_b32_e32 v1, v97
	v_cvt_pk_fp8_f32 v1, v4, v5
	v_mul_f32_e32 v8, 0x42800000, v41
	v_mul_f32_e32 v9, 0x42800000, v61
	v_mul_f32_e32 v4, 0x42800000, v10
	v_cvt_pk_fp8_f32 v1, v8, v9 op_sel:[0,0,1]
	v_mul_f32_e32 v5, 0x42800000, v34
	v_mul_f32_e32 v3, 0x42800000, v3
	ds_write2_b64 v139, v[100:101], v[0:1] offset1:16
	v_mul_f32_e32 v1, 0x42800000, v2
	v_mul_f32_e32 v2, 0x42800000, v6
	v_mov_b32_e32 v0, v97
	v_cvt_pk_fp8_f32 v0, v1, v2
	v_mul_f32_e32 v2, 0x42800000, v14
	v_mov_b32_e32 v1, v97
	v_mul_f32_e32 v6, 0x42800000, v62
	v_cvt_pk_fp8_f32 v0, v4, v5 op_sel:[0,0,1]
	v_mul_f32_e32 v4, 0x42800000, v38
	v_cvt_pk_fp8_f32 v1, v2, v4
	v_mul_f32_e32 v4, 0x42800000, v7
	v_mov_b32_e32 v2, v97
	v_cvt_pk_fp8_f32 v2, v3, v4
	v_mul_f32_e32 v5, 0x42800000, v42
	v_cvt_pk_fp8_f32 v1, v5, v6 op_sel:[0,0,1]
	v_mul_f32_e32 v5, 0x42800000, v11
	v_mul_f32_e32 v6, 0x42800000, v35
	v_cvt_pk_fp8_f32 v2, v5, v6 op_sel:[0,0,1]
	v_mul_f32_e32 v4, 0x42800000, v15
	v_mul_f32_e32 v5, 0x42800000, v39
	v_mov_b32_e32 v3, v97
	v_cvt_pk_fp8_f32 v3, v4, v5
	v_mul_f32_e32 v6, 0x42800000, v43
	v_mul_f32_e32 v7, 0x42800000, v63
	v_cvt_pk_fp8_f32 v3, v6, v7 op_sel:[0,0,1]
	ds_write2_b64 v139, v[0:1], v[2:3] offset0:32 offset1:48
	s_waitcnt vmcnt(15)
	v_mul_f32_e32 v1, 0x42800000, v16
	s_waitcnt vmcnt(14)
	v_mul_f32_e32 v2, 0x42800000, v24
	v_mov_b32_e32 v0, v97
	v_cvt_pk_fp8_f32 v0, v1, v2
	s_waitcnt vmcnt(13)
	v_mul_f32_e32 v3, 0x42800000, v44
	s_waitcnt vmcnt(12)
	v_mul_f32_e32 v4, 0x42800000, v64
	s_waitcnt vmcnt(11)
	v_mul_f32_e32 v2, 0x42800000, v52
	v_cvt_pk_fp8_f32 v0, v3, v4 op_sel:[0,0,1]
	s_waitcnt vmcnt(10)
	v_mul_f32_e32 v3, 0x42800000, v72
	v_mov_b32_e32 v1, v97
	v_cvt_pk_fp8_f32 v1, v2, v3
	s_waitcnt vmcnt(9)
	v_mul_f32_e32 v4, 0x42800000, v80
	s_waitcnt vmcnt(8)
	v_mul_f32_e32 v5, 0x42800000, v88
	v_mul_f32_e32 v3, 0x42800000, v17
	v_cvt_pk_fp8_f32 v1, v4, v5 op_sel:[0,0,1]
	v_mul_f32_e32 v4, 0x42800000, v25
	v_mov_b32_e32 v2, v97
	v_cvt_pk_fp8_f32 v2, v3, v4
	v_mul_f32_e32 v5, 0x42800000, v45
	v_mul_f32_e32 v6, 0x42800000, v65
	v_mul_f32_e32 v4, 0x42800000, v53
	v_cvt_pk_fp8_f32 v2, v5, v6 op_sel:[0,0,1]
	v_mul_f32_e32 v5, 0x42800000, v73
	v_mov_b32_e32 v3, v97
	v_cvt_pk_fp8_f32 v3, v4, v5
	v_mul_f32_e32 v6, 0x42800000, v81
	v_mul_f32_e32 v7, 0x42800000, v89
	v_mul_f32_e32 v4, 0x42800000, v66
	v_cvt_pk_fp8_f32 v3, v6, v7 op_sel:[0,0,1]
	v_mul_f32_e32 v5, 0x42800000, v90
	v_mul_f32_e32 v6, 0x42800000, v67
	v_mul_f32_e32 v7, 0x42800000, v91
	ds_write2_b64 v140, v[0:1], v[2:3] offset1:16
	v_mul_f32_e32 v1, 0x42800000, v18
	v_mul_f32_e32 v2, 0x42800000, v26
	v_mov_b32_e32 v0, v97
	v_cvt_pk_fp8_f32 v0, v1, v2
	v_mul_f32_e32 v3, 0x42800000, v46
	v_mul_f32_e32 v2, 0x42800000, v54
	v_mov_b32_e32 v1, v97
	v_cvt_pk_fp8_f32 v0, v3, v4 op_sel:[0,0,1]
	v_mul_f32_e32 v3, 0x42800000, v74
	v_cvt_pk_fp8_f32 v1, v2, v3
	v_mul_f32_e32 v4, 0x42800000, v82
	v_mul_f32_e32 v3, 0x42800000, v19
	v_mov_b32_e32 v2, v97
	v_cvt_pk_fp8_f32 v1, v4, v5 op_sel:[0,0,1]
	v_mul_f32_e32 v4, 0x42800000, v27
	v_cvt_pk_fp8_f32 v2, v3, v4
	v_mul_f32_e32 v5, 0x42800000, v47
	v_mul_f32_e32 v4, 0x42800000, v55
	v_mov_b32_e32 v3, v97
	v_cvt_pk_fp8_f32 v2, v5, v6 op_sel:[0,0,1]
	v_mul_f32_e32 v5, 0x42800000, v75
	v_cvt_pk_fp8_f32 v3, v4, v5
	v_mul_f32_e32 v6, 0x42800000, v83
	v_cvt_pk_fp8_f32 v3, v6, v7 op_sel:[0,0,1]
	ds_write2_b64 v140, v[0:1], v[2:3] offset0:32 offset1:48
	s_waitcnt vmcnt(7)
	v_mul_f32_e32 v1, 0x42800000, v20
	s_waitcnt vmcnt(6)
	v_mul_f32_e32 v2, 0x42800000, v28
	v_mov_b32_e32 v0, v97
	v_cvt_pk_fp8_f32 v0, v1, v2
	s_waitcnt vmcnt(5)
	v_mul_f32_e32 v3, 0x42800000, v48
	s_waitcnt vmcnt(4)
	v_mul_f32_e32 v4, 0x42800000, v68
	s_waitcnt vmcnt(3)
	v_mul_f32_e32 v2, 0x42800000, v56
	v_cvt_pk_fp8_f32 v0, v3, v4 op_sel:[0,0,1]
	s_waitcnt vmcnt(2)
	v_mul_f32_e32 v3, 0x42800000, v76
	v_mov_b32_e32 v1, v97
	v_cvt_pk_fp8_f32 v1, v2, v3
	s_waitcnt vmcnt(1)
	v_mul_f32_e32 v4, 0x42800000, v84
	s_waitcnt vmcnt(0)
	v_mul_f32_e32 v5, 0x42800000, v92
	v_mul_f32_e32 v3, 0x42800000, v21
	v_cvt_pk_fp8_f32 v1, v4, v5 op_sel:[0,0,1]
	v_mul_f32_e32 v4, 0x42800000, v29
	v_mov_b32_e32 v2, v97
	v_cvt_pk_fp8_f32 v2, v3, v4
	v_mul_f32_e32 v5, 0x42800000, v49
	v_mul_f32_e32 v6, 0x42800000, v69
	v_mul_f32_e32 v4, 0x42800000, v57
	v_cvt_pk_fp8_f32 v2, v5, v6 op_sel:[0,0,1]
	v_mul_f32_e32 v5, 0x42800000, v77
	v_mov_b32_e32 v3, v97
	v_cvt_pk_fp8_f32 v3, v4, v5
	v_mul_f32_e32 v6, 0x42800000, v85
	v_mul_f32_e32 v7, 0x42800000, v93
	v_mul_f32_e32 v4, 0x42800000, v70
	v_cvt_pk_fp8_f32 v3, v6, v7 op_sel:[0,0,1]
	v_mul_f32_e32 v5, 0x42800000, v94
	v_mul_f32_e32 v6, 0x42800000, v71
	v_mul_f32_e32 v7, 0x42800000, v95
	ds_write2_b64 v141, v[0:1], v[2:3] offset1:16
	v_mul_f32_e32 v1, 0x42800000, v22
	v_mul_f32_e32 v2, 0x42800000, v30
	v_mov_b32_e32 v0, v97
	v_cvt_pk_fp8_f32 v0, v1, v2
	v_mul_f32_e32 v3, 0x42800000, v50
	v_mul_f32_e32 v2, 0x42800000, v58
	v_mov_b32_e32 v1, v97
	v_cvt_pk_fp8_f32 v0, v3, v4 op_sel:[0,0,1]
	v_mul_f32_e32 v3, 0x42800000, v78
	v_cvt_pk_fp8_f32 v1, v2, v3
	v_mul_f32_e32 v4, 0x42800000, v86
	v_mul_f32_e32 v3, 0x42800000, v23
	v_mov_b32_e32 v2, v97
	v_cvt_pk_fp8_f32 v1, v4, v5 op_sel:[0,0,1]
	v_mul_f32_e32 v4, 0x42800000, v31
	v_cvt_pk_fp8_f32 v2, v3, v4
	v_mul_f32_e32 v5, 0x42800000, v51
	v_mul_f32_e32 v4, 0x42800000, v59
	v_mov_b32_e32 v3, v97
	v_cvt_pk_fp8_f32 v2, v5, v6 op_sel:[0,0,1]
	v_mul_f32_e32 v5, 0x42800000, v79
	v_cvt_pk_fp8_f32 v3, v4, v5
	v_mul_f32_e32 v6, 0x42800000, v87
	v_cvt_pk_fp8_f32 v3, v6, v7 op_sel:[0,0,1]
	ds_write2_b64 v141, v[0:1], v[2:3] offset0:32 offset1:48
	s_waitcnt lgkmcnt(0)
	s_barrier
	ds_read_b128 v[2:5], v142
	v_add_u32_e32 v8, s8, v102
	s_add_u32 s66, s13, s11
	s_addc_u32 s67, s12, 0
	s_lshl_b32 s6, s10, 7
	s_waitcnt lgkmcnt(0)
	v_cndmask_b32_e64 v6, v2, v4, s[4:5]
	v_cndmask_b32_e64 v4, v4, v2, s[4:5]
	v_lshlrev_b32_e32 v2, 1, v8
	v_and_b32_e32 v2, 0xffffff00, v2
	v_add_u32_e32 v2, s6, v2
	v_or_b32_e32 v2, v2, v103
	v_cndmask_b32_e32 v2, v2, v8, vcc
	v_cndmask_b32_e64 v7, v3, v5, s[4:5]
	v_cndmask_b32_e64 v5, v5, v3, s[4:5]
	v_ashrrev_i32_e32 v3, 31, v2
	v_lshl_add_u64 v[0:1], s[66:67], 0, v[98:99]
	v_lshlrev_b64 v[2:3], 11, v[2:3]
	v_lshl_add_u64 v[2:3], v[0:1], 0, v[2:3]
	global_store_dwordx4 v[2:3], v[4:7], off nt
	ds_read_b128 v[2:5], v143
	v_add_u32_e32 v8, s8, v104
	s_waitcnt lgkmcnt(0)
	v_cndmask_b32_e64 v6, v2, v4, s[4:5]
	v_cndmask_b32_e64 v4, v4, v2, s[4:5]
	v_lshlrev_b32_e32 v2, 1, v8
	v_and_b32_e32 v2, 0xffffff00, v2
	v_add_u32_e32 v2, s6, v2
	v_or_b32_e32 v2, v2, v105
	v_cndmask_b32_e32 v2, v2, v8, vcc
	v_cndmask_b32_e64 v7, v3, v5, s[4:5]
	v_cndmask_b32_e64 v5, v5, v3, s[4:5]
	v_ashrrev_i32_e32 v3, 31, v2
	v_lshlrev_b64 v[2:3], 11, v[2:3]
	v_lshl_add_u64 v[2:3], v[0:1], 0, v[2:3]
	global_store_dwordx4 v[2:3], v[4:7], off nt
	ds_read_b128 v[2:5], v144
	v_add_u32_e32 v8, s8, v106
	s_waitcnt lgkmcnt(0)
	v_cndmask_b32_e64 v6, v2, v4, s[4:5]
	v_cndmask_b32_e64 v4, v4, v2, s[4:5]
	v_lshlrev_b32_e32 v2, 1, v8
	v_and_b32_e32 v2, 0xffffff00, v2
	v_add_u32_e32 v2, s6, v2
	v_or_b32_e32 v2, v2, v107
	v_cndmask_b32_e32 v2, v2, v8, vcc
	v_cndmask_b32_e64 v7, v3, v5, s[4:5]
	v_cndmask_b32_e64 v5, v5, v3, s[4:5]
	v_ashrrev_i32_e32 v3, 31, v2
	v_lshlrev_b64 v[2:3], 11, v[2:3]
	v_lshl_add_u64 v[2:3], v[0:1], 0, v[2:3]
	global_store_dwordx4 v[2:3], v[4:7], off nt
	ds_read_b128 v[2:5], v145
	v_add_u32_e32 v8, s8, v108
	s_waitcnt lgkmcnt(0)
	v_cndmask_b32_e64 v6, v2, v4, s[4:5]
	v_cndmask_b32_e64 v4, v4, v2, s[4:5]
	v_lshlrev_b32_e32 v2, 1, v8
	v_and_b32_e32 v2, 0xffffff00, v2
	v_add_u32_e32 v2, s6, v2
	v_or_b32_e32 v2, v2, v109
	v_cndmask_b32_e32 v2, v2, v8, vcc
	v_cndmask_b32_e64 v7, v3, v5, s[4:5]
	v_cndmask_b32_e64 v5, v5, v3, s[4:5]
	v_ashrrev_i32_e32 v3, 31, v2
	v_lshlrev_b64 v[2:3], 11, v[2:3]
	v_lshl_add_u64 v[2:3], v[0:1], 0, v[2:3]
	global_store_dwordx4 v[2:3], v[4:7], off nt
	ds_read_b128 v[2:5], v146
	v_add_u32_e32 v8, s8, v110
	s_waitcnt lgkmcnt(0)
	v_cndmask_b32_e64 v6, v2, v4, s[4:5]
	v_cndmask_b32_e64 v4, v4, v2, s[4:5]
	v_lshlrev_b32_e32 v2, 1, v8
	v_and_b32_e32 v2, 0xffffff00, v2
	v_add_u32_e32 v2, s6, v2
	v_or_b32_e32 v2, v2, v111
	v_cndmask_b32_e32 v2, v2, v8, vcc
	v_cndmask_b32_e64 v7, v3, v5, s[4:5]
	v_cndmask_b32_e64 v5, v5, v3, s[4:5]
	v_ashrrev_i32_e32 v3, 31, v2
	v_lshlrev_b64 v[2:3], 11, v[2:3]
	v_lshl_add_u64 v[2:3], v[0:1], 0, v[2:3]
	global_store_dwordx4 v[2:3], v[4:7], off nt
	ds_read_b128 v[2:5], v147
	v_add_u32_e32 v8, s8, v112
	s_waitcnt lgkmcnt(0)
	v_cndmask_b32_e64 v6, v2, v4, s[4:5]
	v_cndmask_b32_e64 v4, v4, v2, s[4:5]
	v_lshlrev_b32_e32 v2, 1, v8
	v_and_b32_e32 v2, 0xffffff00, v2
	v_add_u32_e32 v2, s6, v2
	v_or_b32_e32 v2, v2, v113
	v_cndmask_b32_e32 v2, v2, v8, vcc
	v_cndmask_b32_e64 v7, v3, v5, s[4:5]
	v_cndmask_b32_e64 v5, v5, v3, s[4:5]
	v_ashrrev_i32_e32 v3, 31, v2
	v_lshlrev_b64 v[2:3], 11, v[2:3]
	v_lshl_add_u64 v[2:3], v[0:1], 0, v[2:3]
	global_store_dwordx4 v[2:3], v[4:7], off nt
	ds_read_b128 v[2:5], v148
	v_add_u32_e32 v8, s8, v114
	s_waitcnt lgkmcnt(0)
	v_cndmask_b32_e64 v6, v2, v4, s[4:5]
	v_cndmask_b32_e64 v4, v4, v2, s[4:5]
	v_lshlrev_b32_e32 v2, 1, v8
	v_and_b32_e32 v2, 0xffffff00, v2
	v_add_u32_e32 v2, s6, v2
	v_or_b32_e32 v2, v2, v115
	v_cndmask_b32_e32 v2, v2, v8, vcc
	v_cndmask_b32_e64 v7, v3, v5, s[4:5]
	v_cndmask_b32_e64 v5, v5, v3, s[4:5]
	v_ashrrev_i32_e32 v3, 31, v2
	v_lshlrev_b64 v[2:3], 11, v[2:3]
	v_lshl_add_u64 v[2:3], v[0:1], 0, v[2:3]
	global_store_dwordx4 v[2:3], v[4:7], off nt
	ds_read_b128 v[2:5], v149
	v_add_u32_e32 v8, s8, v116
	s_waitcnt lgkmcnt(0)
	v_cndmask_b32_e64 v6, v2, v4, s[4:5]
	v_cndmask_b32_e64 v4, v4, v2, s[4:5]
	v_lshlrev_b32_e32 v2, 1, v8
	v_and_b32_e32 v2, 0xffffff00, v2
	v_add_u32_e32 v2, s6, v2
	v_or_b32_e32 v2, v2, v117
	v_cndmask_b32_e32 v2, v2, v8, vcc
	v_cndmask_b32_e64 v7, v3, v5, s[4:5]
	v_cndmask_b32_e64 v5, v5, v3, s[4:5]
	v_ashrrev_i32_e32 v3, 31, v2
	v_lshlrev_b64 v[2:3], 11, v[2:3]
	v_lshl_add_u64 v[2:3], v[0:1], 0, v[2:3]
	global_store_dwordx4 v[2:3], v[4:7], off nt
	ds_read_b128 v[2:5], v150
	v_add_u32_e32 v8, s8, v118
	s_waitcnt lgkmcnt(0)
	v_cndmask_b32_e64 v6, v2, v4, s[4:5]
	v_cndmask_b32_e64 v4, v4, v2, s[4:5]
	v_lshlrev_b32_e32 v2, 1, v8
	v_and_b32_e32 v2, 0xffffff00, v2
	v_add_u32_e32 v2, s6, v2
	v_or_b32_e32 v2, v2, v119
	v_cndmask_b32_e32 v2, v2, v8, vcc
	v_cndmask_b32_e64 v7, v3, v5, s[4:5]
	v_cndmask_b32_e64 v5, v5, v3, s[4:5]
	v_ashrrev_i32_e32 v3, 31, v2
	v_lshlrev_b64 v[2:3], 11, v[2:3]
	v_lshl_add_u64 v[2:3], v[0:1], 0, v[2:3]
	global_store_dwordx4 v[2:3], v[4:7], off nt
	ds_read_b128 v[2:5], v151
	v_add_u32_e32 v8, s8, v120
	s_waitcnt lgkmcnt(0)
	v_cndmask_b32_e64 v6, v2, v4, s[4:5]
	v_cndmask_b32_e64 v4, v4, v2, s[4:5]
	v_lshlrev_b32_e32 v2, 1, v8
	v_and_b32_e32 v2, 0xffffff00, v2
	v_add_u32_e32 v2, s6, v2
	v_or_b32_e32 v2, v2, v121
	v_cndmask_b32_e32 v2, v2, v8, vcc
	v_cndmask_b32_e64 v7, v3, v5, s[4:5]
	v_cndmask_b32_e64 v5, v5, v3, s[4:5]
	v_ashrrev_i32_e32 v3, 31, v2
	v_lshlrev_b64 v[2:3], 11, v[2:3]
	v_lshl_add_u64 v[2:3], v[0:1], 0, v[2:3]
	global_store_dwordx4 v[2:3], v[4:7], off nt
	ds_read_b128 v[2:5], v152
	v_add_u32_e32 v8, s8, v122
	s_waitcnt lgkmcnt(0)
	v_cndmask_b32_e64 v6, v2, v4, s[4:5]
	v_cndmask_b32_e64 v4, v4, v2, s[4:5]
	v_lshlrev_b32_e32 v2, 1, v8
	v_and_b32_e32 v2, 0xffffff00, v2
	v_add_u32_e32 v2, s6, v2
	v_or_b32_e32 v2, v2, v123
	v_cndmask_b32_e32 v2, v2, v8, vcc
	v_cndmask_b32_e64 v7, v3, v5, s[4:5]
	v_cndmask_b32_e64 v5, v5, v3, s[4:5]
	v_ashrrev_i32_e32 v3, 31, v2
	v_lshlrev_b64 v[2:3], 11, v[2:3]
	v_lshl_add_u64 v[2:3], v[0:1], 0, v[2:3]
	global_store_dwordx4 v[2:3], v[4:7], off nt
	ds_read_b128 v[2:5], v153
	v_add_u32_e32 v8, s8, v124
	s_waitcnt lgkmcnt(0)
	v_cndmask_b32_e64 v6, v2, v4, s[4:5]
	v_cndmask_b32_e64 v4, v4, v2, s[4:5]
	v_lshlrev_b32_e32 v2, 1, v8
	v_and_b32_e32 v2, 0xffffff00, v2
	v_add_u32_e32 v2, s6, v2
	v_or_b32_e32 v2, v2, v125
	v_cndmask_b32_e32 v2, v2, v8, vcc
	v_cndmask_b32_e64 v7, v3, v5, s[4:5]
	v_cndmask_b32_e64 v5, v5, v3, s[4:5]
	v_ashrrev_i32_e32 v3, 31, v2
	v_lshlrev_b64 v[2:3], 11, v[2:3]
	v_lshl_add_u64 v[2:3], v[0:1], 0, v[2:3]
	global_store_dwordx4 v[2:3], v[4:7], off nt
	ds_read_b128 v[2:5], v154
	v_add_u32_e32 v8, s8, v126
	s_waitcnt lgkmcnt(0)
	v_cndmask_b32_e64 v6, v2, v4, s[4:5]
	v_cndmask_b32_e64 v4, v4, v2, s[4:5]
	v_lshlrev_b32_e32 v2, 1, v8
	v_and_b32_e32 v2, 0xffffff00, v2
	v_add_u32_e32 v2, s6, v2
	v_or_b32_e32 v2, v2, v127
	v_cndmask_b32_e32 v2, v2, v8, vcc
	v_cndmask_b32_e64 v7, v3, v5, s[4:5]
	v_cndmask_b32_e64 v5, v5, v3, s[4:5]
	v_ashrrev_i32_e32 v3, 31, v2
	v_lshlrev_b64 v[2:3], 11, v[2:3]
	v_lshl_add_u64 v[2:3], v[0:1], 0, v[2:3]
	global_store_dwordx4 v[2:3], v[4:7], off nt
	ds_read_b128 v[2:5], v155
	v_add_u32_e32 v8, s8, v128
	s_waitcnt lgkmcnt(0)
	v_cndmask_b32_e64 v6, v2, v4, s[4:5]
	v_cndmask_b32_e64 v4, v4, v2, s[4:5]
	v_lshlrev_b32_e32 v2, 1, v8
	v_and_b32_e32 v2, 0xffffff00, v2
	v_add_u32_e32 v2, s6, v2
	v_or_b32_e32 v2, v2, v129
	v_cndmask_b32_e32 v2, v2, v8, vcc
	v_cndmask_b32_e64 v7, v3, v5, s[4:5]
	v_cndmask_b32_e64 v5, v5, v3, s[4:5]
	v_ashrrev_i32_e32 v3, 31, v2
	v_lshlrev_b64 v[2:3], 11, v[2:3]
	v_lshl_add_u64 v[2:3], v[0:1], 0, v[2:3]
	global_store_dwordx4 v[2:3], v[4:7], off nt
	ds_read_b128 v[2:5], v156
	v_add_u32_e32 v8, s8, v130
	s_waitcnt lgkmcnt(0)
	v_cndmask_b32_e64 v6, v2, v4, s[4:5]
	v_cndmask_b32_e64 v4, v4, v2, s[4:5]
	v_lshlrev_b32_e32 v2, 1, v8
	v_and_b32_e32 v2, 0xffffff00, v2
	v_add_u32_e32 v2, s6, v2
	v_or_b32_e32 v2, v2, v131
	v_cndmask_b32_e32 v2, v2, v8, vcc
	v_cndmask_b32_e64 v7, v3, v5, s[4:5]
	v_cndmask_b32_e64 v5, v5, v3, s[4:5]
	v_ashrrev_i32_e32 v3, 31, v2
	v_lshlrev_b64 v[2:3], 11, v[2:3]
	v_lshl_add_u64 v[2:3], v[0:1], 0, v[2:3]
	global_store_dwordx4 v[2:3], v[4:7], off nt
	ds_read_b128 v[2:5], v157
	v_add_u32_e32 v8, s8, v132
	s_waitcnt lgkmcnt(0)
	v_cndmask_b32_e64 v6, v2, v4, s[4:5]
	v_cndmask_b32_e64 v4, v4, v2, s[4:5]
	v_lshlrev_b32_e32 v2, 1, v8
	v_and_b32_e32 v2, 0xffffff00, v2
	v_add_u32_e32 v2, s6, v2
	v_or_b32_e32 v2, v2, v133
	v_cndmask_b32_e32 v2, v2, v8, vcc
	v_cndmask_b32_e64 v7, v3, v5, s[4:5]
	v_cndmask_b32_e64 v5, v5, v3, s[4:5]
	v_ashrrev_i32_e32 v3, 31, v2
	v_lshlrev_b64 v[2:3], 11, v[2:3]
	v_lshl_add_u64 v[0:1], v[0:1], 0, v[2:3]
	global_store_dwordx4 v[0:1], v[4:7], off nt
	s_waitcnt lgkmcnt(0)
	s_barrier
	s_mov_b64 s[6:7], 0
	s_branch .LBB0_593

.LBB0_848:
	s_cmpk_lg_i32 s70, 0x100
	s_cbranch_scc1 .Lcvc_orig
	s_and_b32 s19, s48, 0xff
	s_sub_u32 s20, 0x100, s19
	s_lshl_b32 s21, s19, 1
	s_add_u32 s6, s60, 0xa00
	s_add_u32 s7, s6, 0x100
	s_mov_b32 s44, 0xffff
	s_mov_b32 s45, 0xffff
	s_cmp_eq_u32 s19, 0
	s_cbranch_scc1 .Lcvc_go
	s_cmp_gt_u32 s21, s20
	s_cbranch_scc1 .Lcvc_go
	s_cmp_lt_u32 s60, s19
	s_cbranch_scc1 .LBB0_877
	s_sub_u32 s23, s60, s19
	s_add_u32 s6, s23, 0xa00
	s_add_u32 s7, s6, s20
	s_cmp_lt_u32 s23, s21
	s_cbranch_scc0 .Lcvc_go
	s_add_u32 s44, s7, s20
